# deferred conversion extended to the whole u table (layer-0 rows too) + v layer 1, throttled, 3 slots; plus both gemm3 epilogues pipelined, peer_up select rewrite
# speedup vs baseline: 1.0066x; 1.0034x over previous
.LBB0_34:
	s_andn2_b64 vcc, exec, s[22:23]
	s_cbranch_vccnz .LBB0_38
	s_add_i32 s48, s26, 0xffff5200
	s_and_b32 s49, s48, 0x7fff
	s_cmpk_lt_u32 s48, 0x8000
	s_cbranch_scc1 .LBB0_38
	s_bitcmp1_b32 s49, 14
	s_cbranch_scc1 .LBB0_38
	s_cmpk_lt_u32 s48, 0x8000
	s_cselect_b64 s[22:23], -1, 0
	s_and_b64 s[24:25], s[22:23], exec
	s_cselect_b32 s25, s63, s65
	s_cselect_b32 s24, s62, s64
	s_lshl_b32 s50, s49, 13
	s_add_u32 s24, s24, s50
	s_addc_u32 s25, s25, 0
	v_lshl_add_u64 v[2:3], s[24:25], 0, v[36:37]
	global_load_dwordx4 v[30:33], v36, s[24:25] nt
	global_load_dwordx4 v[26:29], v36, s[24:25] offset:1024 nt
	global_load_dwordx4 v[22:25], v36, s[24:25] offset:2048 nt
	global_load_dwordx4 v[18:21], v36, s[24:25] offset:3072 nt
	v_add_co_u32_e32 v2, vcc, s42, v2
	v_and_b32_e32 v49, 64, v91
	s_nop 0
	v_addc_co_u32_e32 v3, vcc, 0, v3, vcc
	global_load_dwordx4 v[14:17], v[2:3], off nt
	global_load_dwordx4 v[10:13], v[2:3], off offset:1024 nt
	global_load_dwordx4 v[6:9], v[2:3], off offset:2048 nt
	s_nop 0
	global_load_dwordx4 v[2:5], v[2:3], off offset:3072 nt
	v_xor_b32_e32 v92, 1, v91
	v_add_u32_e32 v49, 64, v49
	v_cmp_lt_i32_e32 vcc, v92, v49
	s_waitcnt vmcnt(7)
	v_max_f32_e64 v93, |v33|, |v33|
	v_max_f32_e64 v94, |v32|, |v32|
	s_waitcnt vmcnt(6)
	v_max_f32_e64 v95, |v29|, |v29|
	v_max_f32_e64 v96, |v28|, |v28|
	s_waitcnt vmcnt(5)
	v_max_f32_e64 v97, |v25|, |v25|
	v_max_f32_e64 v98, |v24|, |v24|
	s_waitcnt vmcnt(4)
	v_max_f32_e64 v99, |v21|, |v21|
	v_max_f32_e64 v100, |v20|, |v20|
	v_max_f32_e32 v93, v94, v93
	v_max_f32_e32 v94, v96, v95
	v_max_f32_e32 v95, v98, v97
	v_max_f32_e32 v96, v100, v99
	v_max3_f32 v93, |v30|, |v31|, v93
	v_max3_f32 v94, |v26|, |v27|, v94
	s_waitcnt vmcnt(3)
	v_max_f32_e64 v97, |v17|, |v17|
	v_max_f32_e64 v98, |v16|, |v16|
	s_waitcnt vmcnt(2)
	v_max_f32_e64 v99, |v13|, |v13|
	v_max_f32_e64 v100, |v12|, |v12|
	v_max3_f32 v95, |v22|, |v23|, v95
	v_max3_f32 v96, |v18|, |v19|, v96
	s_waitcnt vmcnt(1)
	v_max_f32_e64 v101, |v9|, |v9|
	v_max_f32_e64 v102, |v8|, |v8|
	s_waitcnt vmcnt(0)
	v_max_f32_e64 v103, |v5|, |v5|
	v_max_f32_e64 v104, |v4|, |v4|
	v_max3_f32 v93, v93, 0, v94
	v_max_f32_e32 v94, v98, v97
	v_max_f32_e32 v97, v100, v99
	v_max_f32_e32 v98, v102, v101
	v_max_f32_e32 v99, v104, v103
	v_max3_f32 v93, v93, v95, v96
	v_max3_f32 v94, |v14|, |v15|, v94
	v_max3_f32 v95, |v10|, |v11|, v97
	v_cndmask_b32_e32 v92, v91, v92, vcc
	v_max3_f32 v96, |v6|, |v7|, v98
	v_max3_f32 v97, |v2|, |v3|, v99
	v_max3_f32 v93, v93, v94, v95
	v_lshlrev_b32_e32 v92, 2, v92
	v_max3_f32 v93, v93, v96, v97
	ds_bpermute_b32 v92, v92, v93
	v_xor_b32_e32 v94, 2, v91
	v_cmp_lt_i32_e32 vcc, v94, v49
	s_waitcnt lgkmcnt(0)
	v_max_f32_e32 v92, v92, v92
	v_cndmask_b32_e32 v94, v91, v94, vcc
	v_lshlrev_b32_e32 v94, 2, v94
	v_max_f32_e32 v92, v93, v92
	ds_bpermute_b32 v93, v94, v92
	v_xor_b32_e32 v94, 4, v91
	v_cmp_lt_i32_e32 vcc, v94, v49
	s_waitcnt lgkmcnt(0)
	v_max_f32_e32 v93, v93, v93
	v_cndmask_b32_e32 v94, v91, v94, vcc
	v_lshlrev_b32_e32 v94, 2, v94
	v_max_f32_e32 v92, v92, v93
	ds_bpermute_b32 v93, v94, v92
	v_xor_b32_e32 v94, 8, v91
	v_cmp_lt_i32_e32 vcc, v94, v49
	s_waitcnt lgkmcnt(0)
	v_max_f32_e32 v93, v93, v93
	v_cndmask_b32_e32 v94, v91, v94, vcc
	v_lshlrev_b32_e32 v94, 2, v94
	v_max_f32_e32 v92, v92, v93
	ds_bpermute_b32 v93, v94, v92
	v_xor_b32_e32 v94, 16, v91
	v_cmp_lt_i32_e32 vcc, v94, v49
	s_waitcnt lgkmcnt(0)
	v_max_f32_e32 v93, v93, v93
	v_cndmask_b32_e32 v94, v91, v94, vcc
	v_lshlrev_b32_e32 v94, 2, v94
	v_max_f32_e32 v92, v92, v93
	ds_bpermute_b32 v93, v94, v92
	v_xor_b32_e32 v94, 32, v91
	v_cmp_lt_i32_e32 vcc, v94, v49
	s_waitcnt lgkmcnt(0)
	v_max_f32_e32 v93, v93, v93
	v_cndmask_b32_e32 v49, v91, v94, vcc
	v_max_f32_e32 v92, v92, v93
	v_lshlrev_b32_e32 v49, 2, v49
	ds_bpermute_b32 v49, v49, v92
	s_waitcnt lgkmcnt(0)
	v_max_f32_e32 v49, v49, v49
	v_max_f32_e32 v49, v92, v49
	s_and_saveexec_b64 s[24:25], s[0:1]
	s_cbranch_execz .LBB0_37
	s_and_b64 s[50:51], s[22:23], exec
	s_mov_b32 s50, 0x12a00000
	s_cselect_b32 s50, s50, 0x12a20000
	s_add_u32 s50, s70, s50
	s_addc_u32 s51, s71, 0
	s_lshl_b32 s49, s49, 2
	v_mul_f32_e32 v92, 0x3b124925, v49
	v_mov_b32_e32 v93, s49
	global_store_dword v93, v92, s[50:51]

.LBB0_611:
	v_readlane_b32 s4, v255, 36
	v_readlane_b32 s8, v252, 0
	s_add_i32 s5, s4, 7
	v_readlane_b32 s9, v252, 1
	s_cmp_ge_i32 s5, s9
	v_readlane_b32 s10, v252, 2
	v_readlane_b32 s11, v252, 3
	s_cbranch_scc1 .LBB0_661
	v_readlane_b32 s4, v255, 34
	s_nop 0
	s_cmp_lg_u32 s4, 0
	s_cbranch_scc1 .Ldfa_done
	s_cmp_gt_u32 s82, 32
	s_cselect_b32 s11, 32, 0
	s_cmp_lt_u32 s2, s11
	s_cbranch_scc1 .Ldfa_done
	s_sub_u32 s10, s82, s11
	s_lshl_b32 s10, s10, 3
	s_sub_u32 s4, s2, s11
	s_lshl_b32 s4, s4, 3
	v_readfirstlane_b32 s11, v0
	s_lshr_b32 s11, s11, 6
	s_add_u32 s4, s4, s11
	s_add_u32 s4, s4, 0x0
	s_cmp_ge_u32 s4, 0x5208
	s_cbranch_scc1 .Ldfa_done
	v_readlane_b32 s6, v252, 4
	v_readlane_b32 s7, v252, 5
	s_nop 0
	s_sub_u32 s6, s6, 0x38
	s_subb_u32 s7, s7, 0
	s_load_dwordx2 s[8:9], s[6:7], 0x0
	s_load_dwordx2 s[6:7], s[6:7], 0x20
	v_and_b32_e32 v6, 63, v0
	v_lshlrev_b32_e32 v7, 4, v6
	v_lshrrev_b32_e32 v56, 5, v6
	v_and_b32_e32 v57, 31, v6
	v_lshlrev_b32_e32 v56, 21, v56
	v_lshl_add_u32 v56, v57, 2, v56
	v_add_u32_e32 v56, 0xaa00000, v56
	s_mov_b64 exec, -1
	s_waitcnt lgkmcnt(0)
	s_lshl_b32 s11, s4, 13
	v_add_u32_e32 v40, s11, v7
	v_add_u32_e32 v41, 0x1000, v40
	global_load_dwordx4 v[8:11], v40, s[8:9] nt
	global_load_dwordx4 v[12:15], v40, s[8:9] offset:1024 nt
	global_load_dwordx4 v[16:19], v40, s[8:9] offset:2048 nt
	global_load_dwordx4 v[20:23], v40, s[8:9] offset:3072 nt
	global_load_dwordx4 v[24:27], v41, s[8:9] nt
	global_load_dwordx4 v[28:31], v41, s[8:9] offset:1024 nt
	global_load_dwordx4 v[32:35], v41, s[8:9] offset:2048 nt
	global_load_dwordx4 v[36:39], v41, s[8:9] offset:3072 nt
.Ldfa_loop:
	s_add_u32 s11, s4, s10
	s_min_u32 s11, s11, 0x5207
	s_mov_b32 s101, s11
	s_lshl_b32 s11, s101, 13
	v_add_u32_e32 v40, s11, v7
	v_add_u32_e32 v41, 0x1000, v40
	global_load_dwordx4 v[76:79], v40, s[8:9] nt
	global_load_dwordx4 v[80:83], v40, s[8:9] offset:1024 nt
	global_load_dwordx4 v[84:87], v40, s[8:9] offset:2048 nt
	global_load_dwordx4 v[88:91], v40, s[8:9] offset:3072 nt
	global_load_dwordx4 v[92:95], v41, s[8:9] nt
	global_load_dwordx4 v[96:99], v41, s[8:9] offset:1024 nt
	global_load_dwordx4 v[100:103], v41, s[8:9] offset:2048 nt
	global_load_dwordx4 v[104:107], v41, s[8:9] offset:3072 nt
	s_waitcnt vmcnt(8)
	v_max3_f32 v42, |v8|, |v9|, |v10|
	v_max3_f32 v43, |v12|, |v13|, |v14|
	v_max3_f32 v44, |v16|, |v17|, |v18|
	v_max3_f32 v45, |v20|, |v21|, |v22|
	v_max3_f32 v46, |v24|, |v25|, |v26|
	v_max3_f32 v47, |v28|, |v29|, |v30|
	v_max3_f32 v48, |v32|, |v33|, |v34|
	v_max3_f32 v49, |v36|, |v37|, |v38|
	v_max_f32_e64 v42, v42, |v11|
	v_max_f32_e64 v43, v43, |v15|
	v_max_f32_e64 v44, v44, |v19|
	v_max_f32_e64 v45, v45, |v23|
	v_max_f32_e64 v46, v46, |v27|
	v_max_f32_e64 v47, v47, |v31|
	v_max_f32_e64 v48, v48, |v35|
	v_max_f32_e64 v49, v49, |v39|
	v_max3_f32 v42, v42, v43, v44
	v_max3_f32 v45, v45, v46, v47
	v_max3_f32 v42, v42, v45, v48
	v_max_f32_e32 v42, v42, v49
	s_nop 1
	v_max_f32_dpp v43, v42, v42 quad_perm:[1,0,3,2] row_mask:0xf bank_mask:0xf bound_ctrl:1
	s_nop 1
	v_max_f32_dpp v42, v43, v43 quad_perm:[2,3,0,1] row_mask:0xf bank_mask:0xf bound_ctrl:1
	s_nop 1
	v_max_f32_dpp v43, v42, v42 row_half_mirror row_mask:0xf bank_mask:0xf bound_ctrl:1
	s_nop 1
	v_max_f32_dpp v42, v43, v43 row_mirror row_mask:0xf bank_mask:0xf bound_ctrl:1
	s_nop 1
	v_mov_b32_e32 v43, v42
	s_nop 1
	v_permlane16_swap_b32_e32 v42, v43
	v_max_f32_e32 v42, v42, v43
	v_mov_b32_e32 v43, v42
	s_nop 1
	v_permlane32_swap_b32_e32 v42, v43
	v_max_f32_e32 v49, v42, v43
	v_mul_f32_e32 v44, 0x3b124925, v49
	s_lshl_b32 s11, s4, 2
	s_add_u32 s11, s11, 0x12a00000
	v_mov_b32_e32 v45, s11
	s_mov_b64 exec, 1
	global_store_dword v45, v44, s[6:7]
	s_mov_b64 exec, -1
	v_mov_b32_e32 v46, 0x43e00000
	v_div_scale_f32 v42, s[100:101], v49, v49, v46
	v_rcp_f32_e32 v43, v42
	s_nop 0
	v_fma_f32 v44, -v42, v43, 1.0
	v_fmac_f32_e32 v43, v44, v43
	v_div_scale_f32 v44, vcc, v46, v49, v46
	v_mul_f32_e32 v45, v44, v43
	v_fma_f32 v47, -v42, v45, v44
	v_fmac_f32_e32 v45, v47, v43
	v_fma_f32 v42, -v42, v45, v44
	s_nop 1
	v_div_fmas_f32 v42, v42, v43, v45
	v_div_fixup_f32 v42, v42, v49, v46
	v_cmp_lt_f32_e32 vcc, 0, v49
	s_nop 1
	v_cndmask_b32_e32 v48, 0, v42, vcc
	v_mul_f32_e32 v8, v8, v48
	v_mul_f32_e32 v9, v9, v48
	v_mul_f32_e32 v10, v10, v48
	v_mul_f32_e32 v11, v11, v48
	v_mul_f32_e32 v12, v12, v48
	v_mul_f32_e32 v13, v13, v48
	v_mul_f32_e32 v14, v14, v48
	v_mul_f32_e32 v15, v15, v48
	v_mul_f32_e32 v16, v16, v48
	v_mul_f32_e32 v17, v17, v48
	v_mul_f32_e32 v18, v18, v48
	v_mul_f32_e32 v19, v19, v48
	v_mul_f32_e32 v20, v20, v48
	v_mul_f32_e32 v21, v21, v48
	v_mul_f32_e32 v22, v22, v48
	v_mul_f32_e32 v23, v23, v48
	v_mul_f32_e32 v24, v24, v48
	v_mul_f32_e32 v25, v25, v48
	v_mul_f32_e32 v26, v26, v48
	v_mul_f32_e32 v27, v27, v48
	v_mul_f32_e32 v28, v28, v48
	v_mul_f32_e32 v29, v29, v48
	v_mul_f32_e32 v30, v30, v48
	v_mul_f32_e32 v31, v31, v48
	v_mul_f32_e32 v32, v32, v48
	v_mul_f32_e32 v33, v33, v48
	v_mul_f32_e32 v34, v34, v48
	v_mul_f32_e32 v35, v35, v48
	v_mul_f32_e32 v36, v36, v48
	v_mul_f32_e32 v37, v37, v48
	v_mul_f32_e32 v38, v38, v48
	v_mul_f32_e32 v39, v39, v48
	v_mov_b32_e32 v58, 0
	v_mov_b32_e32 v59, 0
	v_mov_b32_e32 v60, 0
	v_mov_b32_e32 v61, 0
	v_mov_b32_e32 v62, 0
	v_mov_b32_e32 v63, 0
	v_mov_b32_e32 v64, 0
	v_mov_b32_e32 v65, 0
	v_cvt_pk_fp8_f32 v58, v8, v9
	v_cvt_pk_fp8_f32 v59, v12, v13
	v_cvt_pk_fp8_f32 v60, v16, v17
	v_cvt_pk_fp8_f32 v61, v20, v21
	v_cvt_pk_fp8_f32 v62, v24, v25
	v_cvt_pk_fp8_f32 v63, v28, v29
	v_cvt_pk_fp8_f32 v64, v32, v33
	v_cvt_pk_fp8_f32 v65, v36, v37
	v_cvt_pk_fp8_f32 v58, v10, v11 op_sel:[0,0,1]
	v_cvt_pk_fp8_f32 v59, v14, v15 op_sel:[0,0,1]
	v_cvt_pk_fp8_f32 v60, v18, v19 op_sel:[0,0,1]
	v_cvt_pk_fp8_f32 v61, v22, v23 op_sel:[0,0,1]
	v_cvt_pk_fp8_f32 v62, v26, v27 op_sel:[0,0,1]
	v_cvt_pk_fp8_f32 v63, v30, v31 op_sel:[0,0,1]
	v_cvt_pk_fp8_f32 v64, v34, v35 op_sel:[0,0,1]
	v_cvt_pk_fp8_f32 v65, v38, v39 op_sel:[0,0,1]
	s_and_b32 s11, s4, 0x3fff
	s_lshl_b32 s11, s11, 7
	s_lshr_b32 s101, s4, 14
	s_lshl_b32 s101, s101, 25
	s_add_u32 s11, s11, s101
	v_add_u32_e32 v66, s11, v56
	v_add_u32_e32 v67, 0x400000, v66
	v_add_u32_e32 v68, 0x800000, v66
	v_add_u32_e32 v69, 0xc00000, v66
	v_add_u32_e32 v70, 0x1000000, v66
	v_add_u32_e32 v71, 0x1400000, v66
	v_add_u32_e32 v72, 0x1800000, v66
	v_add_u32_e32 v73, 0x1c00000, v66
	global_store_dword v66, v58, s[6:7] nt
	global_store_dword v67, v59, s[6:7] nt
	global_store_dword v68, v60, s[6:7] nt
	global_store_dword v69, v61, s[6:7] nt
	global_store_dword v70, v62, s[6:7] nt
	global_store_dword v71, v63, s[6:7] nt
	global_store_dword v72, v64, s[6:7] nt
	global_store_dword v73, v65, s[6:7] nt
	s_sleep 127
	s_add_u32 s4, s4, s10
	s_cmp_ge_u32 s4, 0x5208
	s_cbranch_scc1 .Ldfa_done
	s_add_u32 s11, s4, s10
	s_min_u32 s11, s11, 0x5207
	s_mov_b32 s101, s11
	s_lshl_b32 s11, s101, 13
	v_add_u32_e32 v40, s11, v7
	v_add_u32_e32 v41, 0x1000, v40
	global_load_dwordx4 v[8:11], v40, s[8:9] nt
	global_load_dwordx4 v[12:15], v40, s[8:9] offset:1024 nt
	global_load_dwordx4 v[16:19], v40, s[8:9] offset:2048 nt
	global_load_dwordx4 v[20:23], v40, s[8:9] offset:3072 nt
	global_load_dwordx4 v[24:27], v41, s[8:9] nt
	global_load_dwordx4 v[28:31], v41, s[8:9] offset:1024 nt
	global_load_dwordx4 v[32:35], v41, s[8:9] offset:2048 nt
	global_load_dwordx4 v[36:39], v41, s[8:9] offset:3072 nt
	s_waitcnt vmcnt(8)
	v_max3_f32 v42, |v76|, |v77|, |v78|
	v_max3_f32 v43, |v80|, |v81|, |v82|
	v_max3_f32 v44, |v84|, |v85|, |v86|
	v_max3_f32 v45, |v88|, |v89|, |v90|
	v_max3_f32 v46, |v92|, |v93|, |v94|
	v_max3_f32 v47, |v96|, |v97|, |v98|
	v_max3_f32 v48, |v100|, |v101|, |v102|
	v_max3_f32 v49, |v104|, |v105|, |v106|
	v_max_f32_e64 v42, v42, |v79|
	v_max_f32_e64 v43, v43, |v83|
	v_max_f32_e64 v44, v44, |v87|
	v_max_f32_e64 v45, v45, |v91|
	v_max_f32_e64 v46, v46, |v95|
	v_max_f32_e64 v47, v47, |v99|
	v_max_f32_e64 v48, v48, |v103|
	v_max_f32_e64 v49, v49, |v107|
	v_max3_f32 v42, v42, v43, v44
	v_max3_f32 v45, v45, v46, v47
	v_max3_f32 v42, v42, v45, v48
	v_max_f32_e32 v42, v42, v49
	s_nop 1
	v_max_f32_dpp v43, v42, v42 quad_perm:[1,0,3,2] row_mask:0xf bank_mask:0xf bound_ctrl:1
	s_nop 1
	v_max_f32_dpp v42, v43, v43 quad_perm:[2,3,0,1] row_mask:0xf bank_mask:0xf bound_ctrl:1
	s_nop 1
	v_max_f32_dpp v43, v42, v42 row_half_mirror row_mask:0xf bank_mask:0xf bound_ctrl:1
	s_nop 1
	v_max_f32_dpp v42, v43, v43 row_mirror row_mask:0xf bank_mask:0xf bound_ctrl:1
	s_nop 1
	v_mov_b32_e32 v43, v42
	s_nop 1
	v_permlane16_swap_b32_e32 v42, v43
	v_max_f32_e32 v42, v42, v43
	v_mov_b32_e32 v43, v42
	s_nop 1
	v_permlane32_swap_b32_e32 v42, v43
	v_max_f32_e32 v49, v42, v43
	v_mul_f32_e32 v44, 0x3b124925, v49
	s_lshl_b32 s11, s4, 2
	s_add_u32 s11, s11, 0x12a00000
	v_mov_b32_e32 v45, s11
	s_mov_b64 exec, 1
	global_store_dword v45, v44, s[6:7]
	s_mov_b64 exec, -1
	v_mov_b32_e32 v46, 0x43e00000
	v_div_scale_f32 v42, s[100:101], v49, v49, v46
	v_rcp_f32_e32 v43, v42
	s_nop 0
	v_fma_f32 v44, -v42, v43, 1.0
	v_fmac_f32_e32 v43, v44, v43
	v_div_scale_f32 v44, vcc, v46, v49, v46
	v_mul_f32_e32 v45, v44, v43
	v_fma_f32 v47, -v42, v45, v44
	v_fmac_f32_e32 v45, v47, v43
	v_fma_f32 v42, -v42, v45, v44
	s_nop 1
	v_div_fmas_f32 v42, v42, v43, v45
	v_div_fixup_f32 v42, v42, v49, v46
	v_cmp_lt_f32_e32 vcc, 0, v49
	s_nop 1
	v_cndmask_b32_e32 v48, 0, v42, vcc
	v_mul_f32_e32 v76, v76, v48
	v_mul_f32_e32 v77, v77, v48
	v_mul_f32_e32 v78, v78, v48
	v_mul_f32_e32 v79, v79, v48
	v_mul_f32_e32 v80, v80, v48
	v_mul_f32_e32 v81, v81, v48
	v_mul_f32_e32 v82, v82, v48
	v_mul_f32_e32 v83, v83, v48
	v_mul_f32_e32 v84, v84, v48
	v_mul_f32_e32 v85, v85, v48
	v_mul_f32_e32 v86, v86, v48
	v_mul_f32_e32 v87, v87, v48
	v_mul_f32_e32 v88, v88, v48
	v_mul_f32_e32 v89, v89, v48
	v_mul_f32_e32 v90, v90, v48
	v_mul_f32_e32 v91, v91, v48
	v_mul_f32_e32 v92, v92, v48
	v_mul_f32_e32 v93, v93, v48
	v_mul_f32_e32 v94, v94, v48
	v_mul_f32_e32 v95, v95, v48
	v_mul_f32_e32 v96, v96, v48
	v_mul_f32_e32 v97, v97, v48
	v_mul_f32_e32 v98, v98, v48
	v_mul_f32_e32 v99, v99, v48
	v_mul_f32_e32 v100, v100, v48
	v_mul_f32_e32 v101, v101, v48
	v_mul_f32_e32 v102, v102, v48
	v_mul_f32_e32 v103, v103, v48
	v_mul_f32_e32 v104, v104, v48
	v_mul_f32_e32 v105, v105, v48
	v_mul_f32_e32 v106, v106, v48
	v_mul_f32_e32 v107, v107, v48
	v_mov_b32_e32 v58, 0
	v_mov_b32_e32 v59, 0
	v_mov_b32_e32 v60, 0
	v_mov_b32_e32 v61, 0
	v_mov_b32_e32 v62, 0
	v_mov_b32_e32 v63, 0
	v_mov_b32_e32 v64, 0
	v_mov_b32_e32 v65, 0
	v_cvt_pk_fp8_f32 v58, v76, v77
	v_cvt_pk_fp8_f32 v59, v80, v81
	v_cvt_pk_fp8_f32 v60, v84, v85
	v_cvt_pk_fp8_f32 v61, v88, v89
	v_cvt_pk_fp8_f32 v62, v92, v93
	v_cvt_pk_fp8_f32 v63, v96, v97
	v_cvt_pk_fp8_f32 v64, v100, v101
	v_cvt_pk_fp8_f32 v65, v104, v105
	v_cvt_pk_fp8_f32 v58, v78, v79 op_sel:[0,0,1]
	v_cvt_pk_fp8_f32 v59, v82, v83 op_sel:[0,0,1]
	v_cvt_pk_fp8_f32 v60, v86, v87 op_sel:[0,0,1]
	v_cvt_pk_fp8_f32 v61, v90, v91 op_sel:[0,0,1]
	v_cvt_pk_fp8_f32 v62, v94, v95 op_sel:[0,0,1]
	v_cvt_pk_fp8_f32 v63, v98, v99 op_sel:[0,0,1]
	v_cvt_pk_fp8_f32 v64, v102, v103 op_sel:[0,0,1]
	v_cvt_pk_fp8_f32 v65, v106, v107 op_sel:[0,0,1]
	s_and_b32 s11, s4, 0x3fff
	s_lshl_b32 s11, s11, 7
	s_lshr_b32 s101, s4, 14
	s_lshl_b32 s101, s101, 25
	s_add_u32 s11, s11, s101
	v_add_u32_e32 v66, s11, v56
	v_add_u32_e32 v67, 0x400000, v66
	v_add_u32_e32 v68, 0x800000, v66
	v_add_u32_e32 v69, 0xc00000, v66
	v_add_u32_e32 v70, 0x1000000, v66
	v_add_u32_e32 v71, 0x1400000, v66
	v_add_u32_e32 v72, 0x1800000, v66
	v_add_u32_e32 v73, 0x1c00000, v66
	global_store_dword v66, v58, s[6:7] nt
	global_store_dword v67, v59, s[6:7] nt
	global_store_dword v68, v60, s[6:7] nt
	global_store_dword v69, v61, s[6:7] nt
	global_store_dword v70, v62, s[6:7] nt
	global_store_dword v71, v63, s[6:7] nt
	global_store_dword v72, v64, s[6:7] nt
	global_store_dword v73, v65, s[6:7] nt
	s_sleep 127
	s_add_u32 s4, s4, s10
	s_cmp_ge_u32 s4, 0x5208
	s_cbranch_scc1 .Ldfa_done
	s_branch .Ldfa_loop

.LBB0_709:
	v_readlane_b32 s4, v255, 36
	v_readlane_b32 s8, v252, 0
	s_add_i32 s5, s4, 8
	v_readlane_b32 s9, v252, 1
	s_cmp_ge_i32 s5, s9
	v_readlane_b32 s10, v252, 2
	v_readlane_b32 s11, v252, 3
	s_cbranch_scc1 .LBB0_721
	v_readlane_b32 s4, v255, 34
	s_nop 0
	s_cmp_lg_u32 s4, 0
	s_cbranch_scc1 .Ldfb1_done
	s_cmp_gt_u32 s82, 32
	s_cselect_b32 s11, 32, 0
	s_cmp_lt_u32 s2, s11
	s_cbranch_scc1 .Ldfb1_done
	s_sub_u32 s10, s82, s11
	s_lshl_b32 s10, s10, 3
	s_sub_u32 s4, s2, s11
	s_lshl_b32 s4, s4, 3
	v_readfirstlane_b32 s11, v0
	s_lshr_b32 s11, s11, 6
	s_add_u32 s4, s4, s11
	s_add_u32 s4, s4, 0x5208
	s_cmp_ge_u32 s4, 0x8000
	s_cbranch_scc1 .Ldfb1_done
	v_readlane_b32 s6, v252, 4
	v_readlane_b32 s7, v252, 5
	s_nop 0
	s_sub_u32 s6, s6, 0x38
	s_subb_u32 s7, s7, 0
	s_load_dwordx2 s[8:9], s[6:7], 0x0
	s_load_dwordx2 s[6:7], s[6:7], 0x20
	v_and_b32_e32 v6, 63, v0
	v_lshlrev_b32_e32 v7, 4, v6
	v_lshrrev_b32_e32 v56, 5, v6
	v_and_b32_e32 v57, 31, v6
	v_lshlrev_b32_e32 v56, 21, v56
	v_lshl_add_u32 v56, v57, 2, v56
	v_add_u32_e32 v56, 0xaa00000, v56
	s_mov_b64 exec, -1
	s_waitcnt lgkmcnt(0)
	s_lshl_b32 s11, s4, 13
	v_add_u32_e32 v40, s11, v7
	v_add_u32_e32 v41, 0x1000, v40
	global_load_dwordx4 v[8:11], v40, s[8:9] nt
	global_load_dwordx4 v[12:15], v40, s[8:9] offset:1024 nt
	global_load_dwordx4 v[16:19], v40, s[8:9] offset:2048 nt
	global_load_dwordx4 v[20:23], v40, s[8:9] offset:3072 nt
	global_load_dwordx4 v[24:27], v41, s[8:9] nt
	global_load_dwordx4 v[28:31], v41, s[8:9] offset:1024 nt
	global_load_dwordx4 v[32:35], v41, s[8:9] offset:2048 nt
	global_load_dwordx4 v[36:39], v41, s[8:9] offset:3072 nt

.Ldfb1_end:
	v_readlane_b32 s4, v255, 36
	v_readlane_b32 s4, v255, 34
	s_nop 0
	s_cmp_lg_u32 s4, 0
	s_cbranch_scc1 .Ldfb2_done
	s_cmp_gt_u32 s82, 32
	s_cselect_b32 s11, 32, 0
	s_cmp_lt_u32 s2, s11
	s_cbranch_scc1 .Ldfb2_done
	s_sub_u32 s10, s82, s11
	s_lshl_b32 s10, s10, 3
	s_sub_u32 s4, s2, s11
	s_lshl_b32 s4, s4, 3
	v_readfirstlane_b32 s11, v0
	s_lshr_b32 s11, s11, 6
	s_add_u32 s4, s4, s11
	s_add_u32 s4, s4, 0x4000
	s_cmp_ge_u32 s4, 0x4bb8
	s_cbranch_scc1 .Ldfb2_done
	v_readlane_b32 s6, v252, 4
	v_readlane_b32 s7, v252, 5
	s_nop 0
	s_sub_u32 s6, s6, 0x38
	s_subb_u32 s7, s7, 0
	s_load_dwordx2 s[8:9], s[6:7], 0x8
	s_load_dwordx2 s[6:7], s[6:7], 0x20
	v_and_b32_e32 v6, 63, v0
	v_lshlrev_b32_e32 v7, 4, v6
	v_lshrrev_b32_e32 v56, 5, v6
	v_and_b32_e32 v57, 31, v6
	v_lshlrev_b32_e32 v56, 21, v56
	v_lshl_add_u32 v56, v57, 2, v56
	v_add_u32_e32 v56, 0xea00000, v56
	s_mov_b64 exec, -1
	s_waitcnt lgkmcnt(0)
	s_lshl_b32 s11, s4, 13
	v_add_u32_e32 v40, s11, v7
	v_add_u32_e32 v41, 0x1000, v40
	global_load_dwordx4 v[8:11], v40, s[8:9] nt
	global_load_dwordx4 v[12:15], v40, s[8:9] offset:1024 nt
	global_load_dwordx4 v[16:19], v40, s[8:9] offset:2048 nt
	global_load_dwordx4 v[20:23], v40, s[8:9] offset:3072 nt
	global_load_dwordx4 v[24:27], v41, s[8:9] nt
	global_load_dwordx4 v[28:31], v41, s[8:9] offset:1024 nt
	global_load_dwordx4 v[32:35], v41, s[8:9] offset:2048 nt
	global_load_dwordx4 v[36:39], v41, s[8:9] offset:3072 nt
.Ldfb2_loop:
	s_add_u32 s11, s4, s10
	s_min_u32 s11, s11, 0x4bb7
	s_mov_b32 s101, s11
	s_lshl_b32 s11, s101, 13
	v_add_u32_e32 v40, s11, v7
	v_add_u32_e32 v41, 0x1000, v40
	global_load_dwordx4 v[76:79], v40, s[8:9] nt
	global_load_dwordx4 v[80:83], v40, s[8:9] offset:1024 nt
	global_load_dwordx4 v[84:87], v40, s[8:9] offset:2048 nt
	global_load_dwordx4 v[88:91], v40, s[8:9] offset:3072 nt
	global_load_dwordx4 v[92:95], v41, s[8:9] nt
	global_load_dwordx4 v[96:99], v41, s[8:9] offset:1024 nt
	global_load_dwordx4 v[100:103], v41, s[8:9] offset:2048 nt
	global_load_dwordx4 v[104:107], v41, s[8:9] offset:3072 nt
	s_waitcnt vmcnt(8)
	v_max3_f32 v42, |v8|, |v9|, |v10|
	v_max3_f32 v43, |v12|, |v13|, |v14|
	v_max3_f32 v44, |v16|, |v17|, |v18|
	v_max3_f32 v45, |v20|, |v21|, |v22|
	v_max3_f32 v46, |v24|, |v25|, |v26|
	v_max3_f32 v47, |v28|, |v29|, |v30|
	v_max3_f32 v48, |v32|, |v33|, |v34|
	v_max3_f32 v49, |v36|, |v37|, |v38|
	v_max_f32_e64 v42, v42, |v11|
	v_max_f32_e64 v43, v43, |v15|
	v_max_f32_e64 v44, v44, |v19|
	v_max_f32_e64 v45, v45, |v23|
	v_max_f32_e64 v46, v46, |v27|
	v_max_f32_e64 v47, v47, |v31|
	v_max_f32_e64 v48, v48, |v35|
	v_max_f32_e64 v49, v49, |v39|
	v_max3_f32 v42, v42, v43, v44
	v_max3_f32 v45, v45, v46, v47
	v_max3_f32 v42, v42, v45, v48
	v_max_f32_e32 v42, v42, v49
	s_nop 1
	v_max_f32_dpp v43, v42, v42 quad_perm:[1,0,3,2] row_mask:0xf bank_mask:0xf bound_ctrl:1
	s_nop 1
	v_max_f32_dpp v42, v43, v43 quad_perm:[2,3,0,1] row_mask:0xf bank_mask:0xf bound_ctrl:1
	s_nop 1
	v_max_f32_dpp v43, v42, v42 row_half_mirror row_mask:0xf bank_mask:0xf bound_ctrl:1
	s_nop 1
	v_max_f32_dpp v42, v43, v43 row_mirror row_mask:0xf bank_mask:0xf bound_ctrl:1
	s_nop 1
	v_mov_b32_e32 v43, v42
	s_nop 1
	v_permlane16_swap_b32_e32 v42, v43
	v_max_f32_e32 v42, v42, v43
	v_mov_b32_e32 v43, v42
	s_nop 1
	v_permlane32_swap_b32_e32 v42, v43
	v_max_f32_e32 v49, v42, v43
	v_mul_f32_e32 v44, 0x3b124925, v49
	s_lshl_b32 s11, s4, 2
	s_add_u32 s11, s11, 0x12a20000
	v_mov_b32_e32 v45, s11
	s_mov_b64 exec, 1
	global_store_dword v45, v44, s[6:7]
	s_mov_b64 exec, -1
	v_mov_b32_e32 v46, 0x43e00000
	v_div_scale_f32 v42, s[100:101], v49, v49, v46
	v_rcp_f32_e32 v43, v42
	s_nop 0
	v_fma_f32 v44, -v42, v43, 1.0
	v_fmac_f32_e32 v43, v44, v43
	v_div_scale_f32 v44, vcc, v46, v49, v46
	v_mul_f32_e32 v45, v44, v43
	v_fma_f32 v47, -v42, v45, v44
	v_fmac_f32_e32 v45, v47, v43
	v_fma_f32 v42, -v42, v45, v44
	s_nop 1
	v_div_fmas_f32 v42, v42, v43, v45
	v_div_fixup_f32 v42, v42, v49, v46
	v_cmp_lt_f32_e32 vcc, 0, v49
	s_nop 1
	v_cndmask_b32_e32 v48, 0, v42, vcc
	v_mul_f32_e32 v8, v8, v48
	v_mul_f32_e32 v9, v9, v48
	v_mul_f32_e32 v10, v10, v48
	v_mul_f32_e32 v11, v11, v48
	v_mul_f32_e32 v12, v12, v48
	v_mul_f32_e32 v13, v13, v48
	v_mul_f32_e32 v14, v14, v48
	v_mul_f32_e32 v15, v15, v48
	v_mul_f32_e32 v16, v16, v48
	v_mul_f32_e32 v17, v17, v48
	v_mul_f32_e32 v18, v18, v48
	v_mul_f32_e32 v19, v19, v48
	v_mul_f32_e32 v20, v20, v48
	v_mul_f32_e32 v21, v21, v48
	v_mul_f32_e32 v22, v22, v48
	v_mul_f32_e32 v23, v23, v48
	v_mul_f32_e32 v24, v24, v48
	v_mul_f32_e32 v25, v25, v48
	v_mul_f32_e32 v26, v26, v48
	v_mul_f32_e32 v27, v27, v48
	v_mul_f32_e32 v28, v28, v48
	v_mul_f32_e32 v29, v29, v48
	v_mul_f32_e32 v30, v30, v48
	v_mul_f32_e32 v31, v31, v48
	v_mul_f32_e32 v32, v32, v48
	v_mul_f32_e32 v33, v33, v48
	v_mul_f32_e32 v34, v34, v48
	v_mul_f32_e32 v35, v35, v48
	v_mul_f32_e32 v36, v36, v48
	v_mul_f32_e32 v37, v37, v48
	v_mul_f32_e32 v38, v38, v48
	v_mul_f32_e32 v39, v39, v48
	v_mov_b32_e32 v58, 0
	v_mov_b32_e32 v59, 0
	v_mov_b32_e32 v60, 0
	v_mov_b32_e32 v61, 0
	v_mov_b32_e32 v62, 0
	v_mov_b32_e32 v63, 0
	v_mov_b32_e32 v64, 0
	v_mov_b32_e32 v65, 0
	v_cvt_pk_fp8_f32 v58, v8, v9
	v_cvt_pk_fp8_f32 v59, v12, v13
	v_cvt_pk_fp8_f32 v60, v16, v17
	v_cvt_pk_fp8_f32 v61, v20, v21
	v_cvt_pk_fp8_f32 v62, v24, v25
	v_cvt_pk_fp8_f32 v63, v28, v29
	v_cvt_pk_fp8_f32 v64, v32, v33
	v_cvt_pk_fp8_f32 v65, v36, v37
	v_cvt_pk_fp8_f32 v58, v10, v11 op_sel:[0,0,1]
	v_cvt_pk_fp8_f32 v59, v14, v15 op_sel:[0,0,1]
	v_cvt_pk_fp8_f32 v60, v18, v19 op_sel:[0,0,1]
	v_cvt_pk_fp8_f32 v61, v22, v23 op_sel:[0,0,1]
	v_cvt_pk_fp8_f32 v62, v26, v27 op_sel:[0,0,1]
	v_cvt_pk_fp8_f32 v63, v30, v31 op_sel:[0,0,1]
	v_cvt_pk_fp8_f32 v64, v34, v35 op_sel:[0,0,1]
	v_cvt_pk_fp8_f32 v65, v38, v39 op_sel:[0,0,1]
	s_and_b32 s11, s4, 0x3fff
	s_lshl_b32 s11, s11, 7
	s_lshr_b32 s101, s4, 14
	s_lshl_b32 s101, s101, 25
	s_add_u32 s11, s11, s101
	v_add_u32_e32 v66, s11, v56
	v_add_u32_e32 v67, 0x400000, v66
	v_add_u32_e32 v68, 0x800000, v66
	v_add_u32_e32 v69, 0xc00000, v66
	v_add_u32_e32 v70, 0x1000000, v66
	v_add_u32_e32 v71, 0x1400000, v66
	v_add_u32_e32 v72, 0x1800000, v66
	v_add_u32_e32 v73, 0x1c00000, v66
	global_store_dword v66, v58, s[6:7] nt
	global_store_dword v67, v59, s[6:7] nt
	global_store_dword v68, v60, s[6:7] nt
	global_store_dword v69, v61, s[6:7] nt
	global_store_dword v70, v62, s[6:7] nt
	global_store_dword v71, v63, s[6:7] nt
	global_store_dword v72, v64, s[6:7] nt
	global_store_dword v73, v65, s[6:7] nt
	s_sleep 127
	s_add_u32 s4, s4, s10
	s_cmp_ge_u32 s4, 0x4bb8
	s_cbranch_scc1 .Ldfb2_done
	s_add_u32 s11, s4, s10
	s_min_u32 s11, s11, 0x4bb7
	s_mov_b32 s101, s11
	s_lshl_b32 s11, s101, 13
	v_add_u32_e32 v40, s11, v7
	v_add_u32_e32 v41, 0x1000, v40
	global_load_dwordx4 v[8:11], v40, s[8:9] nt
	global_load_dwordx4 v[12:15], v40, s[8:9] offset:1024 nt
	global_load_dwordx4 v[16:19], v40, s[8:9] offset:2048 nt
	global_load_dwordx4 v[20:23], v40, s[8:9] offset:3072 nt
	global_load_dwordx4 v[24:27], v41, s[8:9] nt
	global_load_dwordx4 v[28:31], v41, s[8:9] offset:1024 nt
	global_load_dwordx4 v[32:35], v41, s[8:9] offset:2048 nt
	global_load_dwordx4 v[36:39], v41, s[8:9] offset:3072 nt
	s_waitcnt vmcnt(8)
	v_max3_f32 v42, |v76|, |v77|, |v78|
	v_max3_f32 v43, |v80|, |v81|, |v82|
	v_max3_f32 v44, |v84|, |v85|, |v86|
	v_max3_f32 v45, |v88|, |v89|, |v90|
	v_max3_f32 v46, |v92|, |v93|, |v94|
	v_max3_f32 v47, |v96|, |v97|, |v98|
	v_max3_f32 v48, |v100|, |v101|, |v102|
	v_max3_f32 v49, |v104|, |v105|, |v106|
	v_max_f32_e64 v42, v42, |v79|
	v_max_f32_e64 v43, v43, |v83|
	v_max_f32_e64 v44, v44, |v87|
	v_max_f32_e64 v45, v45, |v91|
	v_max_f32_e64 v46, v46, |v95|
	v_max_f32_e64 v47, v47, |v99|
	v_max_f32_e64 v48, v48, |v103|
	v_max_f32_e64 v49, v49, |v107|
	v_max3_f32 v42, v42, v43, v44
	v_max3_f32 v45, v45, v46, v47
	v_max3_f32 v42, v42, v45, v48
	v_max_f32_e32 v42, v42, v49
	s_nop 1
	v_max_f32_dpp v43, v42, v42 quad_perm:[1,0,3,2] row_mask:0xf bank_mask:0xf bound_ctrl:1
	s_nop 1
	v_max_f32_dpp v42, v43, v43 quad_perm:[2,3,0,1] row_mask:0xf bank_mask:0xf bound_ctrl:1
	s_nop 1
	v_max_f32_dpp v43, v42, v42 row_half_mirror row_mask:0xf bank_mask:0xf bound_ctrl:1
	s_nop 1
	v_max_f32_dpp v42, v43, v43 row_mirror row_mask:0xf bank_mask:0xf bound_ctrl:1
	s_nop 1
	v_mov_b32_e32 v43, v42
	s_nop 1
	v_permlane16_swap_b32_e32 v42, v43
	v_max_f32_e32 v42, v42, v43
	v_mov_b32_e32 v43, v42
	s_nop 1
	v_permlane32_swap_b32_e32 v42, v43
	v_max_f32_e32 v49, v42, v43
	v_mul_f32_e32 v44, 0x3b124925, v49
	s_lshl_b32 s11, s4, 2
	s_add_u32 s11, s11, 0x12a20000
	v_mov_b32_e32 v45, s11
	s_mov_b64 exec, 1
	global_store_dword v45, v44, s[6:7]
	s_mov_b64 exec, -1
	v_mov_b32_e32 v46, 0x43e00000
	v_div_scale_f32 v42, s[100:101], v49, v49, v46
	v_rcp_f32_e32 v43, v42
	s_nop 0
	v_fma_f32 v44, -v42, v43, 1.0
	v_fmac_f32_e32 v43, v44, v43
	v_div_scale_f32 v44, vcc, v46, v49, v46
	v_mul_f32_e32 v45, v44, v43
	v_fma_f32 v47, -v42, v45, v44
	v_fmac_f32_e32 v45, v47, v43
	v_fma_f32 v42, -v42, v45, v44
	s_nop 1
	v_div_fmas_f32 v42, v42, v43, v45
	v_div_fixup_f32 v42, v42, v49, v46
	v_cmp_lt_f32_e32 vcc, 0, v49
	s_nop 1
	v_cndmask_b32_e32 v48, 0, v42, vcc
	v_mul_f32_e32 v76, v76, v48
	v_mul_f32_e32 v77, v77, v48
	v_mul_f32_e32 v78, v78, v48
	v_mul_f32_e32 v79, v79, v48
	v_mul_f32_e32 v80, v80, v48
	v_mul_f32_e32 v81, v81, v48
	v_mul_f32_e32 v82, v82, v48
	v_mul_f32_e32 v83, v83, v48
	v_mul_f32_e32 v84, v84, v48
	v_mul_f32_e32 v85, v85, v48
	v_mul_f32_e32 v86, v86, v48
	v_mul_f32_e32 v87, v87, v48
	v_mul_f32_e32 v88, v88, v48
	v_mul_f32_e32 v89, v89, v48
	v_mul_f32_e32 v90, v90, v48
	v_mul_f32_e32 v91, v91, v48
	v_mul_f32_e32 v92, v92, v48
	v_mul_f32_e32 v93, v93, v48
	v_mul_f32_e32 v94, v94, v48
	v_mul_f32_e32 v95, v95, v48
	v_mul_f32_e32 v96, v96, v48
	v_mul_f32_e32 v97, v97, v48
	v_mul_f32_e32 v98, v98, v48
	v_mul_f32_e32 v99, v99, v48
	v_mul_f32_e32 v100, v100, v48
	v_mul_f32_e32 v101, v101, v48
	v_mul_f32_e32 v102, v102, v48
	v_mul_f32_e32 v103, v103, v48
	v_mul_f32_e32 v104, v104, v48
	v_mul_f32_e32 v105, v105, v48
	v_mul_f32_e32 v106, v106, v48
	v_mul_f32_e32 v107, v107, v48
	v_mov_b32_e32 v58, 0
	v_mov_b32_e32 v59, 0
	v_mov_b32_e32 v60, 0
	v_mov_b32_e32 v61, 0
	v_mov_b32_e32 v62, 0
	v_mov_b32_e32 v63, 0
	v_mov_b32_e32 v64, 0
	v_mov_b32_e32 v65, 0
	v_cvt_pk_fp8_f32 v58, v76, v77
	v_cvt_pk_fp8_f32 v59, v80, v81
	v_cvt_pk_fp8_f32 v60, v84, v85
	v_cvt_pk_fp8_f32 v61, v88, v89
	v_cvt_pk_fp8_f32 v62, v92, v93
	v_cvt_pk_fp8_f32 v63, v96, v97
	v_cvt_pk_fp8_f32 v64, v100, v101
	v_cvt_pk_fp8_f32 v65, v104, v105
	v_cvt_pk_fp8_f32 v58, v78, v79 op_sel:[0,0,1]
	v_cvt_pk_fp8_f32 v59, v82, v83 op_sel:[0,0,1]
	v_cvt_pk_fp8_f32 v60, v86, v87 op_sel:[0,0,1]
	v_cvt_pk_fp8_f32 v61, v90, v91 op_sel:[0,0,1]
	v_cvt_pk_fp8_f32 v62, v94, v95 op_sel:[0,0,1]
	v_cvt_pk_fp8_f32 v63, v98, v99 op_sel:[0,0,1]
	v_cvt_pk_fp8_f32 v64, v102, v103 op_sel:[0,0,1]
	v_cvt_pk_fp8_f32 v65, v106, v107 op_sel:[0,0,1]
	s_and_b32 s11, s4, 0x3fff
	s_lshl_b32 s11, s11, 7
	s_lshr_b32 s101, s4, 14
	s_lshl_b32 s101, s101, 25
	s_add_u32 s11, s11, s101
	v_add_u32_e32 v66, s11, v56
	v_add_u32_e32 v67, 0x400000, v66
	v_add_u32_e32 v68, 0x800000, v66
	v_add_u32_e32 v69, 0xc00000, v66
	v_add_u32_e32 v70, 0x1000000, v66
	v_add_u32_e32 v71, 0x1400000, v66
	v_add_u32_e32 v72, 0x1800000, v66
	v_add_u32_e32 v73, 0x1c00000, v66
	global_store_dword v66, v58, s[6:7] nt
	global_store_dword v67, v59, s[6:7] nt
	global_store_dword v68, v60, s[6:7] nt
	global_store_dword v69, v61, s[6:7] nt
	global_store_dword v70, v62, s[6:7] nt
	global_store_dword v71, v63, s[6:7] nt
	global_store_dword v72, v64, s[6:7] nt
	global_store_dword v73, v65, s[6:7] nt
	s_sleep 127
	s_add_u32 s4, s4, s10
	s_cmp_ge_u32 s4, 0x4bb8
	s_cbranch_scc1 .Ldfb2_done
	s_branch .Ldfb2_loop

.LBB0_856:
	v_readlane_b32 s4, v255, 36
	v_readlane_b32 s8, v252, 0
	s_add_i32 s5, s4, 10
	v_readlane_b32 s9, v252, 1
	s_cmp_ge_i32 s5, s9
	v_readlane_b32 s10, v252, 2
	v_readlane_b32 s11, v252, 3
	s_cbranch_scc1 .LBB0_906
	v_readlane_b32 s4, v255, 34
	s_nop 0
	s_cmp_lg_u32 s4, 0
	s_cbranch_scc1 .Ldfc_done
	s_cmp_gt_u32 s82, 32
	s_cselect_b32 s11, 32, 0
	s_cmp_lt_u32 s2, s11
	s_cbranch_scc1 .Ldfc_done
	s_sub_u32 s10, s82, s11
	s_lshl_b32 s10, s10, 3
	s_sub_u32 s4, s2, s11
	s_lshl_b32 s4, s4, 3
	v_readfirstlane_b32 s11, v0
	s_lshr_b32 s11, s11, 6
	s_add_u32 s4, s4, s11
	s_add_u32 s4, s4, 0x4bb8
	s_cmp_ge_u32 s4, 0x8000
	s_cbranch_scc1 .Ldfc_done
	v_readlane_b32 s6, v252, 4
	v_readlane_b32 s7, v252, 5
	s_nop 0
	s_sub_u32 s6, s6, 0x38
	s_subb_u32 s7, s7, 0
	s_load_dwordx2 s[8:9], s[6:7], 0x8
	s_load_dwordx2 s[6:7], s[6:7], 0x20
	v_and_b32_e32 v6, 63, v0
	v_lshlrev_b32_e32 v7, 4, v6
	v_lshrrev_b32_e32 v56, 5, v6
	v_and_b32_e32 v57, 31, v6
	v_lshlrev_b32_e32 v56, 21, v56
	v_lshl_add_u32 v56, v57, 2, v56
	v_add_u32_e32 v56, 0xea00000, v56
	s_mov_b64 exec, -1
	s_waitcnt lgkmcnt(0)
	s_lshl_b32 s11, s4, 13
	v_add_u32_e32 v40, s11, v7
	v_add_u32_e32 v41, 0x1000, v40
	global_load_dwordx4 v[8:11], v40, s[8:9] nt
	global_load_dwordx4 v[12:15], v40, s[8:9] offset:1024 nt
	global_load_dwordx4 v[16:19], v40, s[8:9] offset:2048 nt
	global_load_dwordx4 v[20:23], v40, s[8:9] offset:3072 nt
	global_load_dwordx4 v[24:27], v41, s[8:9] nt
	global_load_dwordx4 v[28:31], v41, s[8:9] offset:1024 nt
	global_load_dwordx4 v[32:35], v41, s[8:9] offset:2048 nt
	global_load_dwordx4 v[36:39], v41, s[8:9] offset:3072 nt
